# diff attention: rowsum via VALU (no ones-MFMA) + K/V tile staging (address math + LDS-DMA) moved from step top into the PV MFMA shadow
# speedup vs baseline: 1.0087x; 1.0087x over previous
; #define LAS __attribute__((address_space(3)))
; DI void at_stage1(LAS unsigned char* lds, const char* projb, int kcolB, int vcolB, int kt, int slot, int wid, unsigned lb0, unsigned lb1) {
;     const int kv = wid >> 2, sub0 = (wid & 3) * 4;
;     LAS unsigned char* dst = lds + slot * 32768 + kv * 16384 + sub0 * 1024;
;     const char* tb = projb + (size_t)kt * 64 * (INW * 2) + (kv ? vcolB : kcolB);
; #pragma unroll
;     for (int n = 0; n < 4; ++n) { const int sub = sub0 + n;
;         const size_t U = kv ? (size_t)((sub >> 1) * 8) * (INW * 2) + (size_t)((sub & 1) * 128) : (size_t)(sub * 4) * (INW * 2);
;         __builtin_amdgcn_global_load_lds((const unsigned*)(tb + U + ((n & 1) ? lb1 : lb0)), (LAS unsigned*)(dst + n * 1024), 16, 0, 0); }
; }
; DI void attn_unit_diff(const Ctx& C, int l, int b, int h, int j) {
;     ...
;         const int slot = sd % 3;
;         const bool staged = sd + 2 < nt;
;         if (staged) at_stage1(C.lds, projb, kcolB, vcolB, sd + 2, (sd + 2) % 3, wid, lb0, lb1);
;         if (sd <= cw) {
.LBB0_791:
	s_cmp_gt_u32 s94, s67
	s_cbranch_scc1 .LBB0_789

; #define LAS __attribute__((address_space(3)))
; DI float at_softmax(f32x16& p0, f32x16& p1, float& m_run, bool first, bool nearb, LAS const float* tabp, int lane) {
;     ...
; #pragma unroll
;     for (int i = 0; i < 16; ++i) p0[i] = __builtin_amdgcn_exp2f(p0[i]);
; #pragma unroll
;     for (int i = 0; i < 16; ++i) p1[i] = __builtin_amdgcn_exp2f(p1[i]);
;     return alpha;
; }
; DI bf16x8 at_pack(const f32x16& p, int s8) {
;     u32x4 w; w.x = at_cvtpk(p[s8], p[s8 + 1]); w.y = at_cvtpk(p[s8 + 2], p[s8 + 3]); w.z = at_cvtpk(p[s8 + 4], p[s8 + 5]); w.w = at_cvtpk(p[s8 + 6], p[s8 + 7]);
;     return __builtin_bit_cast(bf16x8, w);
; }
; template <int D0> DI void at_pv_block(f32x16 (&o)[4], int vb, const bf16x8 (&pf)[4]) {
;     const s16x4 l0 = at_tr_read<D0 * 512 + 0 * 4096>(vb), h0 = at_tr_read<D0 * 512 + 0 * 4096 + 2048>(vb), l1 = at_tr_read<D0 * 512 + 1 * 4096>(vb), h1 = at_tr_read<D0 * 512 + 1 * 4096 + 2048>(vb);
;     const s16x4 l2 = at_tr_read<D0 * 512 + 2 * 4096>(vb), h2 = at_tr_read<D0 * 512 + 2 * 4096 + 2048>(vb), l3 = at_tr_read<D0 * 512 + 3 * 4096>(vb), h3 = at_tr_read<D0 * 512 + 3 * 4096 + 2048>(vb);
;     asm volatile("s_waitcnt lgkmcnt(0)" ::: "memory"); __builtin_amdgcn_sched_barrier(0);
;     ...
;     o[D0] = MFMA32(AT_PK(l0, h0), pf[0], o[D0]); o[D0] = MFMA32(AT_PK(l1, h1), pf[1], o[D0]); o[D0] = MFMA32(AT_PK(l2, h2), pf[2], o[D0]); o[D0] = MFMA32(AT_PK(l3, h3), pf[3], o[D0]);
; DI void attn_unit_diff(const Ctx& C, int l, int b, int h, int j) {
;     ...
;         if (staged) at_stage1(C.lds, projb, kcolB, vcolB, sd + 2, (sd + 2) % 3, wid, lb0, lb1);
;         if (sd <= cw) {
;             LAS const unsigned char* Kt = C.lds + slot * 32768;
;             const int vb = (int)(size_t)(Kt + 16384) + vrd;
;             const bool nearb = (sd * 64 + 63 - q0w) > -305;
;             LAS const float* tabp = tabl + (sd * 64 - qpos + TABB_OFF + 4 * hi);
;             f32x16 p0, p1;
;             at_qk<KS>(p0, p1, Kt, g * 128, qr, (nearb ? 0.f : cfar) - m_run, r32, hi);
;             const float alpha = at_softmax(p0, p1, m_run, first, nearb, tabp, lane);
;             first = false;
;             if (__any(alpha != 1.f)) {
;                 ol[0] *= alpha;
; #pragma unroll
;                 for (int d0 = 0; d0 < 4; ++d0)
; #pragma unroll
;                     for (int i = 0; i < 16; ++i) o[d0][i] *= alpha;
;             }
;             bf16x8 pf[4];
.LBB0_801:
	v_exp_f32_e32 v2, v113
	v_exp_f32_e32 v6, v117
	v_exp_f32_e32 v7, v118
	v_exp_f32_e32 v8, v119
	v_exp_f32_e32 v9, v120
	v_exp_f32_e32 v10, v121
	v_exp_f32_e32 v11, v122
	v_exp_f32_e32 v12, v123
	v_exp_f32_e32 v13, v124
	v_exp_f32_e32 v113, v96
	v_exp_f32_e32 v100, v100
	v_exp_f32_e32 v101, v101
	v_exp_f32_e32 v102, v102
	v_exp_f32_e32 v103, v103
	v_subrev_u32_e32 v96, s57, v160
	s_mov_b32 s58, s56
	s_mov_b32 s59, s56
	v_exp_f32_e32 v0, v112
	v_exp_f32_e32 v3, v114
	v_exp_f32_e32 v4, v115
	v_exp_f32_e32 v5, v116
	v_exp_f32_e32 v14, v125
	v_exp_f32_e32 v15, v126
	v_exp_f32_e32 v112, v127
	v_exp_f32_e32 v114, v97
	v_exp_f32_e32 v115, v98
	v_exp_f32_e32 v116, v99
	v_add_u32_e32 v117, s49, v96
	v_add_f32_e32 v81, v0, v2
	v_add_f32_e32 v82, v3, v4
	v_add_f32_e32 v83, v5, v6
	v_add_f32_e32 v84, v7, v8
	v_add_f32_e32 v85, v9, v10
	v_add_f32_e32 v86, v11, v12
	v_add_f32_e32 v87, v13, v14
	v_add_f32_e32 v88, v15, v112
	v_add_f32_e32 v89, v113, v114
	v_add_f32_e32 v90, v115, v116
	v_add_f32_e32 v91, v100, v101
	v_add_f32_e32 v92, v102, v103
	v_add_f32_e32 v81, v81, v82
	v_add_f32_e32 v83, v83, v84
	v_add_f32_e32 v85, v85, v86
	v_add_f32_e32 v87, v87, v88
	v_add_f32_e32 v89, v89, v90
	v_add_f32_e32 v91, v91, v92
	v_add_f32_e32 v81, v81, v83
	v_add_f32_e32 v85, v85, v87
	v_add_f32_e32 v89, v89, v91
	v_add_f32_e32 v81, v81, v85
	v_add_f32_e32 v81, v81, v89
	v_cvt_pk_bf16_f32 v96, v0, v2
	v_cvt_pk_bf16_f32 v97, v3, v4
	v_cvt_pk_bf16_f32 v98, v5, v6
	v_cvt_pk_bf16_f32 v99, v7, v8
	v_cvt_pk_bf16_f32 v10, v9, v10
	v_cvt_pk_bf16_f32 v11, v11, v12
	v_cvt_pk_bf16_f32 v12, v13, v14
	v_cvt_pk_bf16_f32 v13, v15, v112
	v_cvt_pk_bf16_f32 v6, v113, v114
	v_cvt_pk_bf16_f32 v7, v115, v116
	v_cvt_pk_bf16_f32 v8, v100, v101
	v_cvt_pk_bf16_f32 v9, v102, v103
	s_mov_b32 s57, s56
	v_exp_f32_e32 v104, v104
	v_exp_f32_e32 v105, v105
	v_exp_f32_e32 v106, v106
	v_exp_f32_e32 v107, v107
	v_exp_f32_e32 v108, v108
	v_exp_f32_e32 v109, v109
	v_exp_f32_e32 v110, v110
	v_exp_f32_e32 v111, v111
	v_cvt_pk_bf16_f32 v2, v104, v105
	v_cvt_pk_bf16_f32 v3, v106, v107
	v_cvt_pk_bf16_f32 v4, v108, v109
	v_cvt_pk_bf16_f32 v5, v110, v111
	v_add_f32_e32 v82, v104, v105
	v_add_f32_e32 v83, v106, v107
	v_add_f32_e32 v84, v108, v109
	v_add_f32_e32 v85, v110, v111
	v_add_f32_e32 v82, v82, v83
	v_add_f32_e32 v84, v84, v85
	v_add_f32_e32 v82, v82, v84
	v_add_f32_e32 v81, v81, v82
	v_add_f32_e32 v80, v80, v81
	ds_read_b64_tr_b16 v[100:101], v117 offset:0
	ds_read_b64_tr_b16 v[102:103], v117 offset:0x800
	ds_read_b64_tr_b16 v[104:105], v117 offset:0x1000
	ds_read_b64_tr_b16 v[106:107], v117 offset:0x1800
	ds_read_b64_tr_b16 v[108:109], v117 offset:0x2000
	ds_read_b64_tr_b16 v[110:111], v117 offset:0x2800
	ds_read_b64_tr_b16 v[112:113], v117 offset:0x3000
	ds_read_b64_tr_b16 v[114:115], v117 offset:0x3800
	s_waitcnt lgkmcnt(0)
	s_nop 0
	s_and_b64 vcc, exec, s[40:41]
	v_mfma_f32_32x32x16_bf16 v[64:79], v[100:103], v[96:99], v[64:79]
	s_mul_hi_u32 s57, s79, 0xaaaaaaab
	s_lshr_b32 s57, s57, 1
	s_mul_i32 s57, s57, 0x18000
	ds_read_b64_tr_b16 v[100:101], v117 offset:0x200
	ds_read_b64_tr_b16 v[102:103], v117 offset:0xa00
	v_mfma_f32_32x32x16_bf16 v[64:79], v[104:107], v[10:13], v[64:79]
	s_sub_i32 s58, s60, s57
	s_sub_i32 s59, s61, s57
	s_add_i32 s58, s49, s58
	v_lshl_add_u64 v[82:83], v[150:151], 0, s[52:53]
	ds_read_b64_tr_b16 v[104:105], v117 offset:0x1200
	ds_read_b64_tr_b16 v[106:107], v117 offset:0x1a00
	v_mfma_f32_32x32x16_bf16 v[64:79], v[108:111], v[6:9], v[64:79]
	s_sub_i32 s80, s4, s57
	s_add_i32 m0, s90, s58
	v_lshl_add_u64 v[84:85], v[82:83], 0, s[36:37]
	s_add_i32 s58, s49, s59
	ds_read_b64_tr_b16 v[108:109], v117 offset:0x2200
	ds_read_b64_tr_b16 v[110:111], v117 offset:0x2a00
	v_mfma_f32_32x32x16_bf16 v[64:79], v[112:115], v[2:5], v[64:79]
	s_sub_i32 s57, s5, s57
	s_cbranch_vccnz .Lstg1_1
	global_load_lds_dwordx4 v[84:85], off
.Lstg1_1:
	ds_read_b64_tr_b16 v[112:113], v117 offset:0x3200
	ds_read_b64_tr_b16 v[114:115], v117 offset:0x3a00
	s_waitcnt lgkmcnt(0)
	v_mfma_f32_32x32x16_bf16 v[48:63], v[100:103], v[96:99], v[48:63]
	v_lshl_add_u64 v[84:85], v[148:149], 0, s[52:53]
	s_add_i32 m0, s90, s58
	s_add_i32 s58, s49, s80
	ds_read_b64_tr_b16 v[100:101], v117 offset:0x400
	ds_read_b64_tr_b16 v[102:103], v117 offset:0xc00
	v_mfma_f32_32x32x16_bf16 v[48:63], v[104:107], v[10:13], v[48:63]
	s_cbranch_vccnz .Lstg1_2
	global_load_lds_dwordx4 v[84:85], off
.Lstg1_2:
	v_lshl_add_u64 v[82:83], v[82:83], 0, s[24:25]
	ds_read_b64_tr_b16 v[104:105], v117 offset:0x1400
	ds_read_b64_tr_b16 v[106:107], v117 offset:0x1c00
	v_mfma_f32_32x32x16_bf16 v[48:63], v[108:111], v[6:9], v[48:63]
	s_add_i32 m0, s90, s58
	s_add_i32 s57, s49, s57
	ds_read_b64_tr_b16 v[108:109], v117 offset:0x2400
	ds_read_b64_tr_b16 v[110:111], v117 offset:0x2c00
	v_mfma_f32_32x32x16_bf16 v[48:63], v[112:115], v[2:5], v[48:63]
	s_cbranch_vccnz .Lstg1_3
	global_load_lds_dwordx4 v[82:83], off
.Lstg1_3:
	ds_read_b64_tr_b16 v[112:113], v117 offset:0x3400
	ds_read_b64_tr_b16 v[114:115], v117 offset:0x3c00
	s_waitcnt lgkmcnt(0)
	v_mfma_f32_32x32x16_bf16 v[32:47], v[100:103], v[96:99], v[32:47]
	v_lshl_add_u64 v[82:83], v[146:147], 0, s[52:53]
	s_add_i32 m0, s90, s57
	ds_read_b64_tr_b16 v[100:101], v117 offset:0x600
	ds_read_b64_tr_b16 v[102:103], v117 offset:0xe00
	v_mfma_f32_32x32x16_bf16 v[32:47], v[104:107], v[10:13], v[32:47]
	s_cbranch_vccnz .Lstg1_4
	global_load_lds_dwordx4 v[82:83], off
.Lstg1_4:
	ds_read_b64_tr_b16 v[104:105], v117 offset:0x1600
	ds_read_b64_tr_b16 v[106:107], v117 offset:0x1e00
	v_mfma_f32_32x32x16_bf16 v[32:47], v[108:111], v[6:9], v[32:47]
	ds_read_b64_tr_b16 v[108:109], v117 offset:0x2600
	ds_read_b64_tr_b16 v[110:111], v117 offset:0x2e00
	v_mfma_f32_32x32x16_bf16 v[32:47], v[112:115], v[2:5], v[32:47]
	ds_read_b64_tr_b16 v[112:113], v117 offset:0x3600
	ds_read_b64_tr_b16 v[114:115], v117 offset:0x3e00
	s_waitcnt lgkmcnt(0)
	v_mfma_f32_32x32x16_bf16 v[16:31], v[100:103], v[96:99], v[16:31]
	s_mov_b64 s[38:39], 0
	v_mfma_f32_32x32x16_bf16 v[16:31], v[104:107], v[10:13], v[16:31]
	v_mfma_f32_32x32x16_bf16 v[16:31], v[108:111], v[6:9], v[16:31]
	v_mfma_f32_32x32x16_bf16 v[16:31], v[112:115], v[2:5], v[16:31]
	s_mov_b64 s[58:59], -1
	s_and_b64 vcc, exec, s[40:41]
	s_cbranch_vccz .LBB0_790

; #define LAS __attribute__((address_space(3)))
; DI void at_stage1(LAS unsigned char* lds, const char* projb, int kcolB, int vcolB, int kt, int slot, int wid, unsigned lb0, unsigned lb1) {
;     const int kv = wid >> 2, sub0 = (wid & 3) * 4;
;     LAS unsigned char* dst = lds + slot * 32768 + kv * 16384 + sub0 * 1024;
;     const char* tb = projb + (size_t)kt * 64 * (INW * 2) + (kv ? vcolB : kcolB);
; #pragma unroll
;     for (int n = 0; n < 4; ++n) { const int sub = sub0 + n;
;         const size_t U = kv ? (size_t)((sub >> 1) * 8) * (INW * 2) + (size_t)((sub & 1) * 128) : (size_t)(sub * 4) * (INW * 2);
;         __builtin_amdgcn_global_load_lds((const unsigned*)(tb + U + ((n & 1) ? lb1 : lb0)), (LAS unsigned*)(dst + n * 1024), 16, 0, 0); }
; }
; DI void attn_unit_diff(const Ctx& C, int l, int b, int h, int j) {
;     ...
;         const int slot = sd % 3;
;         const bool staged = sd + 2 < nt;
;         if (staged) at_stage1(C.lds, projb, kcolB, vcolB, sd + 2, (sd + 2) % 3, wid, lb0, lb1);
;         if (sd <= cw) {
.LBB0_834:
	s_cmp_gt_u32 s35, s7
	s_cbranch_scc1 .LBB0_832

; #define LAS __attribute__((address_space(3)))
; DI float at_softmax(f32x16& p0, f32x16& p1, float& m_run, bool first, bool nearb, LAS const float* tabp, int lane) {
;     ...
; #pragma unroll
;     for (int i = 0; i < 16; ++i) p0[i] = __builtin_amdgcn_exp2f(p0[i]);
; #pragma unroll
;     for (int i = 0; i < 16; ++i) p1[i] = __builtin_amdgcn_exp2f(p1[i]);
;     return alpha;
; }
; DI bf16x8 at_pack(const f32x16& p, int s8) {
;     u32x4 w; w.x = at_cvtpk(p[s8], p[s8 + 1]); w.y = at_cvtpk(p[s8 + 2], p[s8 + 3]); w.z = at_cvtpk(p[s8 + 4], p[s8 + 5]); w.w = at_cvtpk(p[s8 + 6], p[s8 + 7]);
;     return __builtin_bit_cast(bf16x8, w);
; }
; template <int D0> DI void at_pv_block(f32x16 (&o)[4], int vb, const bf16x8 (&pf)[4]) {
;     const s16x4 l0 = at_tr_read<D0 * 512 + 0 * 4096>(vb), h0 = at_tr_read<D0 * 512 + 0 * 4096 + 2048>(vb), l1 = at_tr_read<D0 * 512 + 1 * 4096>(vb), h1 = at_tr_read<D0 * 512 + 1 * 4096 + 2048>(vb);
;     const s16x4 l2 = at_tr_read<D0 * 512 + 2 * 4096>(vb), h2 = at_tr_read<D0 * 512 + 2 * 4096 + 2048>(vb), l3 = at_tr_read<D0 * 512 + 3 * 4096>(vb), h3 = at_tr_read<D0 * 512 + 3 * 4096 + 2048>(vb);
;     asm volatile("s_waitcnt lgkmcnt(0)" ::: "memory"); __builtin_amdgcn_sched_barrier(0);
;     ...
;     o[D0] = MFMA32(AT_PK(l0, h0), pf[0], o[D0]); o[D0] = MFMA32(AT_PK(l1, h1), pf[1], o[D0]); o[D0] = MFMA32(AT_PK(l2, h2), pf[2], o[D0]); o[D0] = MFMA32(AT_PK(l3, h3), pf[3], o[D0]);
; DI void attn_unit_diff(const Ctx& C, int l, int b, int h, int j) {
;     ...
;         if (staged) at_stage1(C.lds, projb, kcolB, vcolB, sd + 2, (sd + 2) % 3, wid, lb0, lb1);
;         if (sd <= cw) {
;             LAS const unsigned char* Kt = C.lds + slot * 32768;
;             const int vb = (int)(size_t)(Kt + 16384) + vrd;
;             const bool nearb = (sd * 64 + 63 - q0w) > -305;
;             LAS const float* tabp = tabl + (sd * 64 - qpos + TABB_OFF + 4 * hi);
;             f32x16 p0, p1;
;             at_qk<KS>(p0, p1, Kt, g * 128, qr, (nearb ? 0.f : cfar) - m_run, r32, hi);
;             const float alpha = at_softmax(p0, p1, m_run, first, nearb, tabp, lane);
;             first = false;
;             if (__any(alpha != 1.f)) {
;                 ol[0] *= alpha;
; #pragma unroll
;                 for (int d0 = 0; d0 < 4; ++d0)
; #pragma unroll
;                     for (int i = 0; i < 16; ++i) o[d0][i] *= alpha;
;             }
;             bf16x8 pf[4];
.LBB0_844:
	v_exp_f32_e32 v2, v113
	v_exp_f32_e32 v6, v117
	v_exp_f32_e32 v7, v118
	v_exp_f32_e32 v8, v119
	v_exp_f32_e32 v9, v120
	v_exp_f32_e32 v10, v121
	v_exp_f32_e32 v11, v122
	v_exp_f32_e32 v12, v123
	v_exp_f32_e32 v13, v124
	v_exp_f32_e32 v113, v96
	v_exp_f32_e32 v100, v100
	v_exp_f32_e32 v101, v101
	v_exp_f32_e32 v102, v102
	v_exp_f32_e32 v103, v103
	v_subrev_u32_e32 v96, s48, v160
	s_mov_b32 s58, s56
	s_mov_b32 s59, s56
	v_exp_f32_e32 v0, v112
	v_exp_f32_e32 v3, v114
	v_exp_f32_e32 v4, v115
	v_exp_f32_e32 v5, v116
	v_exp_f32_e32 v14, v125
	v_exp_f32_e32 v15, v126
	v_exp_f32_e32 v112, v127
	v_exp_f32_e32 v114, v97
	v_exp_f32_e32 v115, v98
	v_exp_f32_e32 v116, v99
	v_add_u32_e32 v117, s31, v96
	v_add_f32_e32 v81, v0, v2
	v_add_f32_e32 v82, v3, v4
	v_add_f32_e32 v83, v5, v6
	v_add_f32_e32 v84, v7, v8
	v_add_f32_e32 v85, v9, v10
	v_add_f32_e32 v86, v11, v12
	v_add_f32_e32 v87, v13, v14
	v_add_f32_e32 v88, v15, v112
	v_add_f32_e32 v89, v113, v114
	v_add_f32_e32 v90, v115, v116
	v_add_f32_e32 v91, v100, v101
	v_add_f32_e32 v92, v102, v103
	v_add_f32_e32 v81, v81, v82
	v_add_f32_e32 v83, v83, v84
	v_add_f32_e32 v85, v85, v86
	v_add_f32_e32 v87, v87, v88
	v_add_f32_e32 v89, v89, v90
	v_add_f32_e32 v91, v91, v92
	v_add_f32_e32 v81, v81, v83
	v_add_f32_e32 v85, v85, v87
	v_add_f32_e32 v89, v89, v91
	v_add_f32_e32 v81, v81, v85
	v_add_f32_e32 v81, v81, v89
	v_cvt_pk_bf16_f32 v96, v0, v2
	v_cvt_pk_bf16_f32 v97, v3, v4
	v_cvt_pk_bf16_f32 v98, v5, v6
	v_cvt_pk_bf16_f32 v99, v7, v8
	v_cvt_pk_bf16_f32 v10, v9, v10
	v_cvt_pk_bf16_f32 v11, v11, v12
	v_cvt_pk_bf16_f32 v12, v13, v14
	v_cvt_pk_bf16_f32 v13, v15, v112
	v_cvt_pk_bf16_f32 v6, v113, v114
	v_cvt_pk_bf16_f32 v7, v115, v116
	v_cvt_pk_bf16_f32 v8, v100, v101
	v_cvt_pk_bf16_f32 v9, v102, v103
	s_mov_b32 s57, s56
	v_exp_f32_e32 v104, v104
	v_exp_f32_e32 v105, v105
	v_exp_f32_e32 v106, v106
	v_exp_f32_e32 v107, v107
	v_exp_f32_e32 v108, v108
	v_exp_f32_e32 v109, v109
	v_exp_f32_e32 v110, v110
	v_exp_f32_e32 v111, v111
	v_cvt_pk_bf16_f32 v2, v104, v105
	v_cvt_pk_bf16_f32 v3, v106, v107
	v_cvt_pk_bf16_f32 v4, v108, v109
	v_cvt_pk_bf16_f32 v5, v110, v111
	v_add_f32_e32 v82, v104, v105
	v_add_f32_e32 v83, v106, v107
	v_add_f32_e32 v84, v108, v109
	v_add_f32_e32 v85, v110, v111
	v_add_f32_e32 v82, v82, v83
	v_add_f32_e32 v84, v84, v85
	v_add_f32_e32 v82, v82, v84
	v_add_f32_e32 v81, v81, v82
	v_add_f32_e32 v80, v80, v81
	ds_read_b64_tr_b16 v[100:101], v117 offset:0
	ds_read_b64_tr_b16 v[102:103], v117 offset:0x800
	ds_read_b64_tr_b16 v[104:105], v117 offset:0x1000
	ds_read_b64_tr_b16 v[106:107], v117 offset:0x1800
	ds_read_b64_tr_b16 v[108:109], v117 offset:0x2000
	ds_read_b64_tr_b16 v[110:111], v117 offset:0x2800
	ds_read_b64_tr_b16 v[112:113], v117 offset:0x3000
	ds_read_b64_tr_b16 v[114:115], v117 offset:0x3800
	s_waitcnt lgkmcnt(0)
	s_nop 0
	s_and_b64 vcc, exec, s[76:77]
	v_mfma_f32_32x32x16_bf16 v[64:79], v[100:103], v[96:99], v[64:79]
	s_mul_hi_u32 s48, s15, 0xaaaaaaab
	s_lshr_b32 s48, s48, 1
	s_mul_i32 s48, s48, 0x18000
	ds_read_b64_tr_b16 v[100:101], v117 offset:0x200
	ds_read_b64_tr_b16 v[102:103], v117 offset:0xa00
	v_mfma_f32_32x32x16_bf16 v[64:79], v[104:107], v[10:13], v[64:79]
	s_sub_i32 s49, s60, s48
	s_sub_i32 s57, s61, s48
	s_add_i32 s49, s31, s49
	v_lshl_add_u64 v[82:83], v[150:151], 0, s[52:53]
	ds_read_b64_tr_b16 v[104:105], v117 offset:0x1200
	ds_read_b64_tr_b16 v[106:107], v117 offset:0x1a00
	v_mfma_f32_32x32x16_bf16 v[64:79], v[108:111], v[6:9], v[64:79]
	s_sub_i32 s58, s4, s48
	s_add_i32 m0, s90, s49
	v_lshl_add_u64 v[84:85], v[82:83], 0, s[36:37]
	s_add_i32 s49, s31, s57
	ds_read_b64_tr_b16 v[108:109], v117 offset:0x2200
	ds_read_b64_tr_b16 v[110:111], v117 offset:0x2a00
	v_mfma_f32_32x32x16_bf16 v[64:79], v[112:115], v[2:5], v[64:79]
	s_sub_i32 s48, s5, s48
	s_cbranch_vccnz .Lstg2_1
	global_load_lds_dwordx4 v[84:85], off
.Lstg2_1:
	ds_read_b64_tr_b16 v[112:113], v117 offset:0x3200
	ds_read_b64_tr_b16 v[114:115], v117 offset:0x3a00
	s_waitcnt lgkmcnt(0)
	v_mfma_f32_32x32x16_bf16 v[48:63], v[100:103], v[96:99], v[48:63]
	v_lshl_add_u64 v[84:85], v[148:149], 0, s[52:53]
	s_add_i32 m0, s90, s49
	s_add_i32 s49, s31, s58
	ds_read_b64_tr_b16 v[100:101], v117 offset:0x400
	ds_read_b64_tr_b16 v[102:103], v117 offset:0xc00
	v_mfma_f32_32x32x16_bf16 v[48:63], v[104:107], v[10:13], v[48:63]
	s_cbranch_vccnz .Lstg2_2
	global_load_lds_dwordx4 v[84:85], off
.Lstg2_2:
	v_lshl_add_u64 v[82:83], v[82:83], 0, s[24:25]
	ds_read_b64_tr_b16 v[104:105], v117 offset:0x1400
	ds_read_b64_tr_b16 v[106:107], v117 offset:0x1c00
	v_mfma_f32_32x32x16_bf16 v[48:63], v[108:111], v[6:9], v[48:63]
	s_add_i32 m0, s90, s49
	s_add_i32 s48, s31, s48
	ds_read_b64_tr_b16 v[108:109], v117 offset:0x2400
	ds_read_b64_tr_b16 v[110:111], v117 offset:0x2c00
	v_mfma_f32_32x32x16_bf16 v[48:63], v[112:115], v[2:5], v[48:63]
	s_cbranch_vccnz .Lstg2_3
	global_load_lds_dwordx4 v[82:83], off
.Lstg2_3:
	ds_read_b64_tr_b16 v[112:113], v117 offset:0x3400
	ds_read_b64_tr_b16 v[114:115], v117 offset:0x3c00
	s_waitcnt lgkmcnt(0)
	v_mfma_f32_32x32x16_bf16 v[32:47], v[100:103], v[96:99], v[32:47]
	v_lshl_add_u64 v[82:83], v[146:147], 0, s[52:53]
	s_add_i32 m0, s90, s48
	ds_read_b64_tr_b16 v[100:101], v117 offset:0x600
	ds_read_b64_tr_b16 v[102:103], v117 offset:0xe00
	v_mfma_f32_32x32x16_bf16 v[32:47], v[104:107], v[10:13], v[32:47]
	s_cbranch_vccnz .Lstg2_4
	global_load_lds_dwordx4 v[82:83], off
.Lstg2_4:
	ds_read_b64_tr_b16 v[104:105], v117 offset:0x1600
	ds_read_b64_tr_b16 v[106:107], v117 offset:0x1e00
	v_mfma_f32_32x32x16_bf16 v[32:47], v[108:111], v[6:9], v[32:47]
	ds_read_b64_tr_b16 v[108:109], v117 offset:0x2600
	ds_read_b64_tr_b16 v[110:111], v117 offset:0x2e00
	v_mfma_f32_32x32x16_bf16 v[32:47], v[112:115], v[2:5], v[32:47]
	ds_read_b64_tr_b16 v[112:113], v117 offset:0x3600
	ds_read_b64_tr_b16 v[114:115], v117 offset:0x3e00
	s_waitcnt lgkmcnt(0)
	v_mfma_f32_32x32x16_bf16 v[16:31], v[100:103], v[96:99], v[16:31]
	s_mov_b64 s[42:43], 0
	v_mfma_f32_32x32x16_bf16 v[16:31], v[104:107], v[10:13], v[16:31]
	v_mfma_f32_32x32x16_bf16 v[16:31], v[108:111], v[6:9], v[16:31]
	v_mfma_f32_32x32x16_bf16 v[16:31], v[112:115], v[2:5], v[16:31]
	s_mov_b64 s[58:59], -1
	s_and_b64 vcc, exec, s[76:77]
	s_cbranch_vccz .LBB0_833
